# static priority raise for waves 4-7 (second wave of each SIMD) through the P0 weight-conversion loop, reset at the end of P0
# speedup vs baseline: 1.0027x; 1.0027x over previous
.LBB0_168:
	s_andn2_b64 vcc, exec, s[4:5]
	s_cbranch_vccnz .LBB0_182
	v_lshrrev_b32_e32 v1, 1, v67
	s_and_b32 s30, s1, 15
	v_and_b32_e32 v1, 24, v1
	v_lshl_or_b32 v8, s30, 7, v1
	v_lshlrev_b32_e32 v2, 2, v67
	v_and_b32_e32 v66, 60, v2
	v_mul_u32_u24_e32 v2, s27, v8
	s_mov_b32 s9, 0
	s_lshl_b32 s8, s29, 8
	v_mov_b32_e32 v131, 0
	v_lshlrev_b32_e32 v130, 2, v2
	v_lshl_add_u64 v[2:3], s[18:19], 0, v[130:131]
	s_lshl_b64 s[6:7], s[8:9], 2
	s_lshl_b32 s8, s27, 2
	v_lshl_add_u64 v[4:5], v[2:3], 0, s[6:7]
	v_lshlrev_b32_e32 v130, 2, v66
	v_lshl_add_u64 v[2:3], v[2:3], 0, s[8:9]
	s_add_i32 s1, s27, s27
	v_lshl_add_u64 v[4:5], v[4:5], 0, v[130:131]
	v_lshl_add_u64 v[6:7], v[2:3], 0, s[6:7]
	s_add_i32 s1, s1, s27
	v_lshl_add_u64 v[6:7], v[6:7], 0, v[130:131]
	global_load_dwordx4 v[58:61], v[4:5], off nt
	global_load_dwordx4 v[62:65], v[6:7], off nt
	v_mov_b32_e32 v4, s1
	v_mad_u32_u24 v6, v8, s27, v4
	v_lshlrev_b32_e32 v4, 2, v6
	v_mov_b32_e32 v5, v131
	v_lshl_add_u64 v[2:3], v[2:3], 0, s[8:9]
	v_lshl_add_u64 v[4:5], s[18:19], 0, v[4:5]
	v_lshl_add_u64 v[2:3], v[2:3], 0, s[6:7]
	v_lshl_add_u64 v[4:5], v[4:5], 0, s[6:7]
	v_lshl_add_u64 v[2:3], v[2:3], 0, v[130:131]
	v_lshl_add_u64 v[4:5], v[4:5], 0, v[130:131]
	global_load_dwordx4 v[50:53], v[2:3], off nt
	global_load_dwordx4 v[42:45], v[4:5], off nt
	v_add_u32_e32 v4, s27, v6
	v_lshlrev_b32_e32 v2, 2, v4
	v_mov_b32_e32 v3, v131
	v_lshl_add_u64 v[2:3], s[18:19], 0, v[2:3]
	v_add_u32_e32 v4, s27, v4
	v_mov_b32_e32 v5, v131
	v_lshl_add_u64 v[2:3], v[2:3], 0, s[6:7]
	v_lshl_add_u64 v[6:7], v[4:5], 2, s[18:19]
	v_lshl_add_u64 v[2:3], v[2:3], 0, v[130:131]
	v_lshl_add_u64 v[6:7], v[6:7], 0, s[6:7]
	v_lshl_add_u64 v[6:7], v[6:7], 0, v[130:131]
	global_load_dwordx4 v[54:57], v[2:3], off nt
	global_load_dwordx4 v[34:37], v[6:7], off nt
	v_add_u32_e32 v2, s27, v4
	v_mov_b32_e32 v3, v131
	v_lshl_add_u64 v[4:5], v[2:3], 2, s[18:19]
	v_add_u32_e32 v2, s27, v2
	v_lshl_add_u64 v[4:5], v[4:5], 0, s[6:7]
	v_lshl_add_u64 v[6:7], v[2:3], 2, s[18:19]
	v_mad_u64_u32 v[2:3], s[2:3], s27, 25, v[2:3]
	v_lshl_add_u64 v[4:5], v[4:5], 0, v[130:131]
	v_lshl_add_u64 v[6:7], v[6:7], 0, s[6:7]
	v_mov_b32_e32 v3, v131
	v_lshl_add_u64 v[6:7], v[6:7], 0, v[130:131]
	global_load_dwordx4 v[38:41], v[4:5], off nt
	global_load_dwordx4 v[46:49], v[6:7], off nt
	v_lshl_add_u64 v[4:5], v[2:3], 2, s[18:19]
	v_add_u32_e32 v12, s27, v2
	v_mov_b32_e32 v13, v131
	v_lshl_add_u64 v[4:5], v[4:5], 0, s[6:7]
	v_lshl_add_u64 v[2:3], v[12:13], 2, s[18:19]
	v_lshl_add_u64 v[10:11], v[4:5], 0, v[130:131]
	v_lshl_add_u64 v[2:3], v[2:3], 0, s[6:7]
	v_lshl_add_u64 v[14:15], v[2:3], 0, v[130:131]
	global_load_dwordx4 v[2:5], v[10:11], off nt
	global_load_dwordx4 v[6:9], v[14:15], off nt
	v_add_u32_e32 v10, s27, v12
	v_mov_b32_e32 v11, v131
	v_lshl_add_u64 v[12:13], v[10:11], 2, s[18:19]
	v_add_u32_e32 v20, s27, v10
	v_mov_b32_e32 v21, v131
	v_lshl_add_u64 v[12:13], v[12:13], 0, s[6:7]
	v_lshl_add_u64 v[10:11], v[20:21], 2, s[18:19]
	v_lshl_add_u64 v[18:19], v[12:13], 0, v[130:131]
	v_lshl_add_u64 v[10:11], v[10:11], 0, s[6:7]
	v_lshl_add_u64 v[22:23], v[10:11], 0, v[130:131]
	global_load_dwordx4 v[10:13], v[18:19], off nt
	global_load_dwordx4 v[14:17], v[22:23], off nt
	v_add_u32_e32 v18, s27, v20
	v_mov_b32_e32 v19, v131
	v_lshl_add_u64 v[20:21], v[18:19], 2, s[18:19]
	v_add_u32_e32 v28, s27, v18
	v_mov_b32_e32 v29, v131
	v_lshl_add_u64 v[20:21], v[20:21], 0, s[6:7]
	v_lshl_add_u64 v[18:19], v[28:29], 2, s[18:19]
	v_lshl_add_u64 v[26:27], v[20:21], 0, v[130:131]
	v_lshl_add_u64 v[18:19], v[18:19], 0, s[6:7]
	v_lshl_add_u64 v[30:31], v[18:19], 0, v[130:131]
	global_load_dwordx4 v[18:21], v[26:27], off nt
	global_load_dwordx4 v[22:25], v[30:31], off nt
	v_add_u32_e32 v26, s27, v28
	v_mov_b32_e32 v27, v131
	v_lshl_add_u64 v[28:29], v[26:27], 2, s[18:19]
	v_add_u32_e32 v26, s27, v26
	v_lshl_add_u64 v[28:29], v[28:29], 0, s[6:7]
	v_lshl_add_u64 v[26:27], v[26:27], 2, s[18:19]
	v_lshl_add_u64 v[68:69], v[28:29], 0, v[130:131]
	v_lshl_add_u64 v[26:27], v[26:27], 0, s[6:7]
	v_lshl_add_u64 v[70:71], v[26:27], 0, v[130:131]
	global_load_dwordx4 v[26:29], v[68:69], off nt
	global_load_dwordx4 v[30:33], v[70:71], off nt
	v_bfe_u32 v200, v67, 3, 3
	v_lshlrev_b32_e32 v70, 1, v67
	v_lshlrev_b32_e32 v75, 7, v200
	v_bfe_u32 v68, v67, 4, 2
	v_and_b32_e32 v71, 14, v70
	v_and_b32_e32 v76, 0x80, v75
	v_or_b32_e32 v90, 8, v200
	v_bitop3_b32 v70, v70, v68, 14 bitop3:0x6c
	v_bitop3_b32 v73, v68, v71, 4 bitop3:0x36
	v_bitop3_b32 v74, v68, v71, 8 bitop3:0x36
	v_bitop3_b32 v71, v68, v71, 12 bitop3:0x36
	v_or_b32_e32 v91, 16, v200
	v_or_b32_e32 v201, v76, v68
	v_lshrrev_b32_e32 v68, 1, v90
	v_or_b32_e32 v203, 24, v200
	v_or_b32_e32 v202, v68, v76
	v_lshrrev_b32_e32 v68, 1, v91
	v_or_b32_e32 v92, 32, v200
	v_or_b32_e32 v210, v68, v76
	v_lshrrev_b32_e32 v68, 1, v203
	v_or_b32_e32 v205, 40, v200
	v_or_b32_e32 v211, v68, v76
	v_lshrrev_b32_e32 v68, 1, v92
	v_or_b32_e32 v228, 48, v200
	v_or_b32_e32 v212, v68, v76
	v_lshrrev_b32_e32 v68, 1, v205
	v_or_b32_e32 v232, 56, v200
	v_or_b32_e32 v213, v68, v76
	v_lshrrev_b32_e32 v68, 1, v228
	v_or_b32_e32 v214, v68, v76
	v_lshrrev_b32_e32 v68, 1, v232
	v_or_b32_e32 v215, v68, v76
	v_or_b32_e32 v68, 64, v200
	v_lshrrev_b32_e32 v68, 1, v68
	v_or_b32_e32 v217, v68, v76
	v_or_b32_e32 v68, 0x48, v200
	v_lshrrev_b32_e32 v68, 1, v68
	v_or_b32_e32 v219, v68, v76
	v_or_b32_e32 v68, 0x50, v200
	v_lshrrev_b32_e32 v68, 1, v68
	v_or_b32_e32 v221, v68, v76
	v_or_b32_e32 v68, 0x58, v200
	v_lshrrev_b32_e32 v68, 1, v68
	v_or_b32_e32 v223, v68, v76
	v_or_b32_e32 v68, 0x60, v200
	v_lshrrev_b32_e32 v68, 1, v68
	v_or_b32_e32 v225, v68, v76
	v_or_b32_e32 v68, 0x68, v200
	v_lshrrev_b32_e32 v68, 1, v68
	v_or_b32_e32 v227, v68, v76
	v_or_b32_e32 v68, 0x70, v200
	v_lshrrev_b32_e32 v68, 1, v68
	v_or_b32_e32 v229, v68, v76
	v_or_b32_e32 v68, 0x78, v200
	v_lshrrev_b32_e32 v68, 1, v68
	v_or_b32_e32 v231, v68, v76
	v_or_b32_e32 v68, 0x80, v200
	v_lshrrev_b32_e32 v68, 1, v68
	v_or_b32_e32 v233, v68, v76
	v_or_b32_e32 v68, 0x88, v200
	v_lshrrev_b32_e32 v68, 1, v68
	v_or_b32_e32 v235, v68, v76
	v_or_b32_e32 v68, 0x90, v200
	v_lshrrev_b32_e32 v68, 1, v68
	v_or_b32_e32 v237, v68, v76
	v_or_b32_e32 v68, 0x98, v200
	v_lshrrev_b32_e32 v68, 1, v68
	v_or_b32_e32 v239, v68, v76
	v_or_b32_e32 v68, 0xa0, v200
	v_lshrrev_b32_e32 v68, 1, v68
	v_or_b32_e32 v241, v68, v76
	v_or_b32_e32 v68, 0xa8, v200
	v_lshrrev_b32_e32 v68, 1, v68
	v_or_b32_e32 v243, v68, v76
	v_or_b32_e32 v68, 0xb0, v200
	v_lshrrev_b32_e32 v68, 1, v68
	v_or_b32_e32 v245, v68, v76
	v_or_b32_e32 v68, 0xb8, v200
	v_lshrrev_b32_e32 v68, 1, v68
	v_or_b32_e32 v247, v68, v76
	v_or_b32_e32 v68, 0xc0, v200
	v_lshrrev_b32_e32 v68, 1, v68
	v_or_b32_e32 v249, v68, v76
	v_or_b32_e32 v68, 0xc8, v200
	v_lshrrev_b32_e32 v68, 1, v68
	v_or_b32_e32 v251, v68, v76
	v_or_b32_e32 v68, 0xd0, v200
	v_lshrrev_b32_e32 v68, 1, v68
	v_or_b32_e32 v253, v68, v76
	v_or_b32_e32 v68, 0xd8, v200
	v_lshrrev_b32_e32 v68, 1, v68
	v_or_b32_e32 v218, v68, v76
	v_or_b32_e32 v68, 0xe0, v200
	s_lshl_b32 s0, s0, 7
	v_lshrrev_b32_e32 v68, 1, v68
	s_and_b32 s0, s0, 0xffffe000
	v_or_b32_e32 v222, v68, v76
	v_or_b32_e32 v68, 0xe8, v200
	s_add_i32 s0, s0, 0
	v_lshlrev_b32_e32 v69, 9, v67
	v_lshrrev_b32_e32 v68, 1, v68
	v_and_b32_e32 v72, 63, v67
	s_add_i32 s0, s0, 0x10000
	v_and_b32_e32 v69, 0x1e00, v69
	v_or_b32_e32 v226, v68, v76
	v_or_b32_e32 v68, 0xf0, v200
	v_add_u32_e32 v69, s0, v69
	v_lshlrev_b32_e32 v72, 4, v72
	s_movk_i32 s1, 0x70
	v_add_u32_e32 v75, s0, v75
	v_bfe_u32 v67, v67, 1, 5
	v_lshl_add_u32 v77, v90, 7, s0
	v_lshlrev_b32_e32 v78, 2, v90
	v_lshl_add_u32 v79, v91, 7, s0
	v_lshlrev_b32_e32 v80, 2, v91
	v_lshl_add_u32 v81, v203, 7, s0
	v_lshlrev_b32_e32 v82, 2, v203
	v_lshl_add_u32 v83, v92, 7, s0
	v_lshl_add_u32 v84, v205, 7, s0
	v_lshlrev_b32_e32 v85, 2, v205
	v_lshl_add_u32 v86, v228, 7, s0
	v_lshlrev_b32_e32 v87, 2, v228
	v_lshl_add_u32 v88, v232, 7, s0
	v_lshlrev_b32_e32 v89, 2, v232
	v_lshrrev_b32_e32 v68, 1, v68
	s_add_u32 s0, s68, 0x7e000000
	v_and_b32_e32 v132, 0x70, v72
	v_bitop3_b32 v67, v67, s1, v72 bitop3:0x48
	v_bitop3_b32 v78, v78, s1, v72 bitop3:0x48
	v_bitop3_b32 v80, v80, s1, v72 bitop3:0x48
	v_bitop3_b32 v82, v82, s1, v72 bitop3:0x48
	v_bitop3_b32 v85, v85, s1, v72 bitop3:0x48
	v_bitop3_b32 v87, v87, s1, v72 bitop3:0x48
	v_bitop3_b32 v72, v89, s1, v72 bitop3:0x48
	v_or_b32_e32 v230, v68, v76
	v_or_b32_e32 v68, 0xf8, v200
	s_addc_u32 s1, s69, 0
	v_lshlrev_b32_e32 v70, 3, v70
	v_lshlrev_b32_e32 v73, 3, v73
	v_lshlrev_b32_e32 v74, 3, v74
	v_lshlrev_b32_e32 v71, 3, v71
	v_lshrrev_b32_e32 v68, 1, v68
	s_add_u32 s2, s68, 0x5e000000
	v_mov_b32_e32 v133, v131
	v_or_b32_e32 v234, v68, v76
	s_addc_u32 s3, s69, 0
	v_lshlrev_b32_e32 v130, 2, v66
	v_add_u32_e32 v236, v69, v70
	v_add_u32_e32 v238, v69, v73
	v_add_u32_e32 v240, v69, v74
	v_add_u32_e32 v242, v69, v71
	v_add_u32_e32 v244, v75, v67
	v_add_u32_e32 v246, v77, v78
	v_add_u32_e32 v248, v79, v80
	v_add_u32_e32 v250, v81, v82
	v_add_u32_e32 v252, v83, v67
	v_add_u32_e32 v204, v84, v85
	v_add_u32_e32 v216, v86, v87
	v_add_u32_e32 v220, v88, v72
	v_cmp_gt_u32_e32 vcc, 0x100, v0
	s_cbranch_vccnz .Lconv_prio0
	s_setprio 1
.Lconv_prio0:
	s_branch .LBB0_171
.LBB0_170:
	s_waitcnt vmcnt(11)
	v_mul_f32_e32 v106, 0x42800000, v106
	s_waitcnt vmcnt(10)
	v_mul_f32_e32 v110, 0x42800000, v110
	v_mov_b32_e32 v137, v131
	v_cvt_pk_fp8_f32 v137, v106, v110
	s_waitcnt vmcnt(9)
	v_mul_f32_e32 v98, 0x42800000, v98
	s_waitcnt vmcnt(8)
	v_mul_f32_e32 v102, 0x42800000, v102
	v_mov_b32_e32 v106, v131
	v_cvt_pk_fp8_f32 v137, v98, v102 op_sel:[0,0,1]
	v_mul_f32_e32 v98, 0x42800000, v115
	v_mul_f32_e32 v102, 0x42800000, v119
	v_cvt_pk_fp8_f32 v106, v98, v102
	v_mul_f32_e32 v98, 0x42800000, v107
	v_mul_f32_e32 v102, 0x42800000, v111
	v_mov_b32_e32 v107, v131
	v_cvt_pk_fp8_f32 v107, v98, v102
	v_mul_f32_e32 v98, 0x42800000, v99
	v_mul_f32_e32 v99, 0x42800000, v103
	v_mul_f32_e32 v102, 0x42800000, v120
	v_cvt_pk_fp8_f32 v107, v98, v99 op_sel:[0,0,1]
	v_mul_f32_e32 v99, 0x42800000, v116
	v_mov_b32_e32 v98, v131
	v_cvt_pk_fp8_f32 v98, v99, v102
	v_mul_f32_e32 v102, 0x42800000, v108
	v_mul_f32_e32 v108, 0x42800000, v112
	v_mov_b32_e32 v99, v131
	v_cvt_pk_fp8_f32 v99, v102, v108
	v_mul_f32_e32 v114, 0x42800000, v114
	v_mul_f32_e32 v118, 0x42800000, v118
	v_mov_b32_e32 v136, v131
	v_cvt_pk_fp8_f32 v136, v114, v118
	v_mul_f32_e32 v110, 0x42800000, v123
	v_mul_f32_e32 v114, 0x42800000, v127
	v_cvt_pk_fp8_f32 v106, v110, v114 op_sel:[0,0,1]
	v_mul_f32_e32 v103, 0x42800000, v124
	v_mul_f32_e32 v110, 0x42800000, v128
	v_mul_f32_e32 v100, 0x42800000, v100
	v_mul_f32_e32 v102, 0x42800000, v104
	v_cvt_pk_fp8_f32 v98, v103, v110 op_sel:[0,0,1]
	v_cvt_pk_fp8_f32 v99, v100, v102 op_sel:[0,0,1]
	v_mul_f32_e32 v100, 0x42800000, v117
	v_mul_f32_e32 v103, 0x42800000, v121
	v_mov_b32_e32 v102, v131
	v_cvt_pk_fp8_f32 v102, v100, v103
	v_mul_f32_e32 v100, 0x42800000, v109
	v_mul_f32_e32 v109, 0x42800000, v113
	v_mov_b32_e32 v103, v131
	v_cvt_pk_fp8_f32 v103, v100, v109
	v_mul_f32_e32 v100, 0x42800000, v101
	v_mul_f32_e32 v101, 0x42800000, v105
	s_waitcnt vmcnt(3)
	v_mul_f32_e32 v66, 0x42800000, v66
	v_cvt_pk_fp8_f32 v103, v100, v101 op_sel:[0,0,1]
	s_waitcnt vmcnt(2)
	v_mul_f32_e32 v70, 0x42800000, v70
	v_mov_b32_e32 v101, v131
	v_cvt_pk_fp8_f32 v101, v66, v70
	v_mul_f32_e32 v74, 0x42800000, v74
	v_mul_f32_e32 v78, 0x42800000, v78
	v_mov_b32_e32 v100, v131
	s_waitcnt vmcnt(1)
	v_mul_f32_e32 v66, 0x42800000, v90
	s_waitcnt vmcnt(0)
	v_mul_f32_e32 v70, 0x42800000, v94
	v_cvt_pk_fp8_f32 v100, v74, v78
	v_cvt_pk_fp8_f32 v101, v66, v70 op_sel:[0,0,1]
	v_mul_f32_e32 v70, 0x42800000, v75
	v_mul_f32_e32 v74, 0x42800000, v79
	v_mov_b32_e32 v66, v131
	v_cvt_pk_fp8_f32 v66, v70, v74
	v_mul_f32_e32 v70, 0x42800000, v67
	v_mul_f32_e32 v71, 0x42800000, v71
	v_mov_b32_e32 v67, v131
	v_cvt_pk_fp8_f32 v67, v70, v71
	v_mul_f32_e32 v70, 0x42800000, v91
	v_mul_f32_e32 v71, 0x42800000, v95
	v_mul_f32_e32 v74, 0x42800000, v80
	v_cvt_pk_fp8_f32 v67, v70, v71 op_sel:[0,0,1]
	v_mul_f32_e32 v71, 0x42800000, v76
	v_mov_b32_e32 v70, v131
	v_cvt_pk_fp8_f32 v70, v71, v74
	v_mul_f32_e32 v68, 0x42800000, v68
	v_mul_f32_e32 v72, 0x42800000, v72
	v_mov_b32_e32 v71, v131
	v_cvt_pk_fp8_f32 v71, v68, v72
	v_mul_f32_e32 v68, 0x42800000, v92
	v_mul_f32_e32 v72, 0x42800000, v96
	v_mul_f32_e32 v74, 0x42800000, v81
	v_cvt_pk_fp8_f32 v71, v68, v72 op_sel:[0,0,1]
	v_mul_f32_e32 v72, 0x42800000, v77
	v_mov_b32_e32 v68, v131
	v_cvt_pk_fp8_f32 v68, v72, v74
	v_mul_f32_e32 v72, 0x42800000, v69
	v_mul_f32_e32 v73, 0x42800000, v73
	v_mov_b32_e32 v69, v131
	v_mul_f32_e32 v122, 0x42800000, v122
	v_mul_f32_e32 v126, 0x42800000, v126
	v_cvt_pk_fp8_f32 v69, v72, v73
	v_cvt_pk_fp8_f32 v136, v122, v126 op_sel:[0,0,1]
	v_mul_f32_e32 v104, 0x42800000, v125
	v_mul_f32_e32 v108, 0x42800000, v129
	v_mul_f32_e32 v75, 0x42800000, v83
	v_mul_f32_e32 v78, 0x42800000, v87
	v_cvt_pk_fp8_f32 v102, v104, v108 op_sel:[0,0,1]
	v_mul_f32_e32 v82, 0x42800000, v82
	v_mul_f32_e32 v86, 0x42800000, v86
	v_cvt_pk_fp8_f32 v66, v75, v78 op_sel:[0,0,1]
	v_mul_f32_e32 v75, 0x42800000, v84
	v_mul_f32_e32 v76, 0x42800000, v88
	v_cvt_pk_fp8_f32 v100, v82, v86 op_sel:[0,0,1]
	v_cvt_pk_fp8_f32 v70, v75, v76 op_sel:[0,0,1]
	v_mul_f32_e32 v75, 0x42800000, v85
	v_mul_f32_e32 v76, 0x42800000, v89
	v_mul_f32_e32 v72, 0x42800000, v93
	v_mul_f32_e32 v73, 0x42800000, v97
	v_cvt_pk_fp8_f32 v68, v75, v76 op_sel:[0,0,1]
	v_cvt_pk_fp8_f32 v69, v72, v73 op_sel:[0,0,1]
	ds_write2_b64 v240, v[136:137], v[106:107] offset1:16
	ds_write2_b64 v240, v[98:99], v[102:103] offset0:32 offset1:48
	ds_write2_b64 v242, v[100:101], v[66:67] offset1:16
	ds_write2_b64 v242, v[70:71], v[68:69] offset0:32 offset1:48
	ds_read_b128 v[66:69], v244
	v_or_b32_e32 v70, 0xc0, v200
	v_cndmask_b32_e64 v70, v249, v70, s[6:7]
	v_or_b32_e32 v70, s8, v70
	v_mov_b32_e32 v71, v131
	v_lshlrev_b64 v[70:71], 11, v[70:71]
	v_lshl_add_u64 v[74:75], v[134:135], 0, v[70:71]
	ds_read_b128 v[70:73], v246
	s_waitcnt lgkmcnt(1)
	global_store_dwordx4 v[74:75], v[66:69], off nt
	v_readfirstlane_b32 s22, v224
	s_andn2_b64 vcc, exec, s[10:11]
	v_or_b32_e32 v66, 0xc8, v200
	v_cndmask_b32_e64 v66, v251, v66, s[6:7]
	v_or_b32_e32 v66, s8, v66
	v_mov_b32_e32 v67, v131
	v_lshlrev_b64 v[66:67], 11, v[66:67]
	v_lshl_add_u64 v[66:67], v[134:135], 0, v[66:67]
	s_waitcnt lgkmcnt(0)
	global_store_dwordx4 v[66:67], v[70:73], off nt
	ds_read_b128 v[66:69], v248
	s_mov_b64 s[18:19], s[12:13]
	v_or_b32_e32 v70, 0xd0, v200
	v_cndmask_b32_e64 v70, v253, v70, s[6:7]
	v_or_b32_e32 v70, s8, v70
	v_mov_b32_e32 v71, v131
	v_lshlrev_b64 v[70:71], 11, v[70:71]
	v_lshl_add_u64 v[74:75], v[134:135], 0, v[70:71]
	ds_read_b128 v[70:73], v250
	s_waitcnt lgkmcnt(1)
	global_store_dwordx4 v[74:75], v[66:69], off nt
	s_mov_b64 s[20:21], s[14:15]
	s_mov_b32 s27, s26
	v_or_b32_e32 v66, 0xd8, v200
	v_cndmask_b32_e64 v66, v218, v66, s[6:7]
	v_or_b32_e32 v66, s8, v66
	v_mov_b32_e32 v67, v131
	v_lshlrev_b64 v[66:67], 11, v[66:67]
	v_lshl_add_u64 v[66:67], v[134:135], 0, v[66:67]
	s_waitcnt lgkmcnt(0)
	global_store_dwordx4 v[66:67], v[70:73], off nt
	ds_read_b128 v[66:69], v252
	s_mov_b32 s30, s4
	v_or_b32_e32 v70, 0xe0, v200
	v_cndmask_b32_e64 v70, v222, v70, s[6:7]
	v_or_b32_e32 v70, s8, v70
	v_mov_b32_e32 v71, v131
	v_lshlrev_b64 v[70:71], 11, v[70:71]
	v_lshl_add_u64 v[74:75], v[134:135], 0, v[70:71]
	ds_read_b128 v[70:73], v204
	s_waitcnt lgkmcnt(1)
	global_store_dwordx4 v[74:75], v[66:69], off nt
	s_mov_b32 s29, s24
	s_mov_b32 s28, s25
	v_or_b32_e32 v66, 0xe8, v200
	v_cndmask_b32_e64 v66, v226, v66, s[6:7]
	v_or_b32_e32 v66, s8, v66
	v_mov_b32_e32 v67, v131
	v_lshlrev_b64 v[66:67], 11, v[66:67]
	v_lshl_add_u64 v[66:67], v[134:135], 0, v[66:67]
	s_waitcnt lgkmcnt(0)
	global_store_dwordx4 v[66:67], v[70:73], off nt
	ds_read_b128 v[66:69], v216
	s_nop 0
	v_or_b32_e32 v70, 0xf0, v200
	v_cndmask_b32_e64 v70, v230, v70, s[6:7]
	v_or_b32_e32 v70, s8, v70
	v_mov_b32_e32 v71, v131
	v_lshlrev_b64 v[70:71], 11, v[70:71]
	v_lshl_add_u64 v[74:75], v[134:135], 0, v[70:71]
	ds_read_b128 v[70:73], v220
	s_waitcnt lgkmcnt(1)
	global_store_dwordx4 v[74:75], v[66:69], off nt
	s_nop 1
	v_or_b32_e32 v66, 0xf8, v200
	v_cndmask_b32_e64 v66, v234, v66, s[6:7]
	v_or_b32_e32 v66, s8, v66
	v_mov_b32_e32 v67, v131
	v_lshlrev_b64 v[66:67], 11, v[66:67]
	v_lshl_add_u64 v[66:67], v[134:135], 0, v[66:67]
	s_waitcnt lgkmcnt(0)
	global_store_dwordx4 v[66:67], v[70:73], off nt
	s_cbranch_vccz .LBB0_182

.LBB0_182:
	s_setprio 0
	v_readlane_b32 s0, v254, 1
	s_cmp_gt_i32 s0, 1
	s_cselect_b64 s[6:7], -1, 0
	s_and_b64 s[0:1], s[52:53], s[6:7]
	s_andn2_b64 vcc, exec, s[0:1]
	s_cbranch_vccnz .LBB0_227
	s_waitcnt vmcnt(0)
	s_barrier
	s_mov_b64 s[8:9], exec
	v_readlane_b32 s0, v254, 4
	v_readlane_b32 s1, v254, 5
	s_and_b64 s[0:1], s[8:9], s[0:1]
	s_mov_b64 exec, s[0:1]
	s_cbranch_execz .LBB0_226
	v_readlane_b32 s0, v254, 6
	s_waitcnt vmcnt(0) expcnt(0) lgkmcnt(0)
	s_nop 0
	v_mov_b32_e32 v1, s0
	ds_read_b32 v3, v1
	ds_read_b32 v1, v1 offset:4
	s_waitcnt lgkmcnt(1)
	v_cmp_ne_u32_e32 vcc, 0, v3
	s_cbranch_vccnz .LBB0_197
	v_readlane_b32 s2, v254, 2
	v_readlane_b32 s3, v254, 3
	s_add_u32 s10, s76, 0x1000
	s_load_dwordx2 s[0:1], s[2:3], 0x4
	s_addc_u32 s11, s77, 0
	s_add_u32 s12, s76, 0x1100
	s_addc_u32 s13, s77, 0
	s_add_u32 s14, s76, 0x1200
	s_addc_u32 s15, s77, 0
	s_waitcnt lgkmcnt(0)
	s_mul_i32 s0, s0, s74
	s_add_u32 s16, s76, 0x1300
	s_mul_i32 s0, s0, s1
	s_addc_u32 s17, s77, 0
	s_mov_b32 s1, 1
	v_mov_b32_e32 v17, 0
	s_branch .LBB0_187
